# p4+p10+p3 edits with cold s_nop padding so every MFMA loop sits at baseline address + k*256 B (removes the 4-mod-8 code shift)
# speedup vs baseline: 1.0167x; 1.0003x over previous
_Z6mk_fwd4Args:
	s_nop 0
	s_nop 0
	s_nop 0
	s_nop 0
	s_nop 0
	s_nop 0
	s_nop 0
	s_nop 0
	s_nop 0
	s_nop 0
	s_nop 0
	s_nop 0
	s_nop 0
	s_nop 0
	s_nop 0
	s_nop 0
	s_nop 0
	s_nop 0
	s_nop 0
	s_nop 0
	s_nop 0
	s_nop 0
	s_nop 0
	s_nop 0
	s_nop 0
	s_nop 0
	s_nop 0
	s_nop 0
	s_nop 0
	s_nop 0
	s_nop 0
	s_nop 0
	s_nop 0
	s_nop 0
	s_nop 0
	s_nop 0
	s_nop 0
	s_nop 0
	s_nop 0
	s_nop 0
	s_nop 0
	s_nop 0
	s_nop 0
	s_nop 0
	s_nop 0
	s_nop 0
	s_nop 0
	s_nop 0
	s_nop 0
	s_nop 0
	s_nop 0
	s_nop 0
	s_nop 0
	s_nop 0
	s_nop 0
	s_nop 0
	s_nop 0
	s_nop 0
	s_nop 0
	s_nop 0
	s_nop 0
	s_nop 0
	s_nop 0
	s_mov_b32 s100, -1
	s_load_dword s84, s[0:1], 0xd0
	s_load_dwordx4 s[4:7], s[0:1], 0xc0
	s_mov_b32 s87, s2
	s_add_u32 s2, s0, 0xd0
	s_addc_u32 s3, s1, 0
	v_readfirstlane_b32 s92, v0
	s_waitcnt lgkmcnt(0)
	v_writelane_b32 v242, s4, 0
	s_mov_b32 s93, s87
	s_nop 0
	v_writelane_b32 v242, s5, 1
	v_writelane_b32 v242, s6, 2
	v_writelane_b32 v242, s7, 3
	v_writelane_b32 v242, s2, 4
	s_nop 1
	v_writelane_b32 v242, s3, 5
	s_and_b32 s3, s84, 7
	s_mov_b32 s2, 0
	s_cmp_lg_u32 s3, 0
	s_cbranch_scc1 .LBB0_2
	s_ashr_i32 s4, s87, 31
	s_lshr_b32 s4, s4, 29
	s_add_i32 s4, s87, s4
	s_and_b32 s5, s4, -8
	s_ashr_i32 s3, s84, 3
	s_sub_i32 s5, s87, s5
	s_mul_i32 s3, s3, s5
	s_ashr_i32 s4, s4, 3
	s_add_i32 s93, s3, s4

.LBB0_397:
	v_lshl_add_u64 v[90:91], s[8:9], 0, v[34:35]
	v_mbcnt_lo_u32_b32 v35, -1, 0
	v_mbcnt_hi_u32_b32 v35, -1, v35
	v_and_b32_e32 v38, 64, v35
	v_xor_b32_e32 v37, 16, v35
	v_add_u32_e32 v38, 64, v38
	v_cmp_lt_i32_e32 vcc, v37, v38
	v_and_b32_e32 v36, 0xf0, v34
	v_and_b32_e32 v34, 48, v0
	v_cndmask_b32_e32 v37, v35, v37, vcc
	v_lshlrev_b32_e32 v144, 2, v37
	v_xor_b32_e32 v37, 32, v35
	v_cmp_lt_i32_e32 vcc, v37, v38
	v_add_u32_e32 v36, 0, v36
	v_add_u32_e32 v34, 0, v34
	v_cndmask_b32_e32 v35, v35, v37, vcc
	v_lshlrev_b32_e32 v145, 2, v35
	v_mul_u32_u24_e32 v35, 0x110, v141
	v_mul_u32_u24_e32 v37, 0x110, v1
	v_or_b32_e32 v143, s10, v1
	s_mov_b32 s7, 0
	s_lshl_b32 s15, s84, 4
	v_add_u32_e32 v146, v36, v35
	v_lshlrev_b32_e32 v92, 1, v148
	v_mov_b32_e32 v95, 0
	s_movk_i32 s16, 0x3000
	s_mov_b64 s[8:9], 0x1800
	s_movk_i32 s17, 0x1000
	v_add_u32_e32 v147, v34, v37
	v_mov_b32_e32 v149, 0x358637bd
	s_mov_b32 s18, 0x800000
	s_mov_b32 s20, s87
	s_branch .LBB0_399
	s_nop 0
	s_nop 0
	s_nop 0
	s_nop 0
	s_nop 0
	s_nop 0
	s_nop 0
	s_nop 0
	s_nop 0
	s_nop 0
	s_nop 0
	s_nop 0
	s_nop 0
	s_nop 0
	s_nop 0
	s_nop 0
	s_nop 0
	s_nop 0
	s_nop 0
	s_nop 0
	s_nop 0
	s_nop 0
	s_nop 0
	s_nop 0
	s_nop 0
	s_nop 0
	s_nop 0
	s_nop 0
	s_nop 0

.LBB0_405:
	s_waitcnt vmcnt(31)
	v_lshlrev_b32_e32 v78, 16, v66
	v_and_b32_e32 v79, 0xffff0000, v66
	v_lshlrev_b32_e32 v80, 16, v67
	v_and_b32_e32 v81, 0xffff0000, v67
	s_waitcnt vmcnt(30)
	v_lshlrev_b32_e32 v74, 16, v64
	v_and_b32_e32 v75, 0xffff0000, v64
	v_lshlrev_b32_e32 v76, 16, v65
	v_and_b32_e32 v77, 0xffff0000, v65
	s_waitcnt vmcnt(29)
	v_lshlrev_b32_e32 v70, 16, v62
	v_and_b32_e32 v71, 0xffff0000, v62
	v_lshlrev_b32_e32 v72, 16, v63
	v_and_b32_e32 v73, 0xffff0000, v63
	s_waitcnt vmcnt(28)
	v_lshlrev_b32_e32 v66, 16, v60
	v_and_b32_e32 v67, 0xffff0000, v60
	v_lshlrev_b32_e32 v68, 16, v61
	v_and_b32_e32 v69, 0xffff0000, v61
	s_waitcnt vmcnt(23)
	v_lshlrev_b32_e32 v62, 16, v58
	v_and_b32_e32 v63, 0xffff0000, v58
	v_lshlrev_b32_e32 v64, 16, v59
	v_and_b32_e32 v65, 0xffff0000, v59
	s_waitcnt vmcnt(22)
	v_lshlrev_b32_e32 v58, 16, v54
	v_and_b32_e32 v59, 0xffff0000, v54
	v_lshlrev_b32_e32 v60, 16, v55
	v_and_b32_e32 v61, 0xffff0000, v55
	s_waitcnt vmcnt(21)
	v_lshlrev_b32_e32 v54, 16, v56
	v_and_b32_e32 v55, 0xffff0000, v56
	v_lshlrev_b32_e32 v56, 16, v57
	v_and_b32_e32 v57, 0xffff0000, v57
	s_waitcnt vmcnt(20)
	v_lshlrev_b32_e32 v50, 16, v138
	v_and_b32_e32 v51, 0xffff0000, v138
	v_lshlrev_b32_e32 v52, 16, v139
	s_andn2_b64 vcc, exec, s[12:13]
	v_and_b32_e32 v53, 0xffff0000, v139
	s_cbranch_vccnz .LBB0_398
	ds_read_b128 v[150:153], v147
	ds_read_b128 v[154:157], v147 offset:64
	s_waitcnt lgkmcnt(1)
	v_mfma_f32_16x16x32_bf16 v[78:81], v[150:153], v[34:37], v[78:81]
	ds_read_b128 v[150:153], v147 offset:4352
	ds_read_b128 v[158:161], v147 offset:4416
	s_waitcnt lgkmcnt(1)
	v_mfma_f32_16x16x32_bf16 v[74:77], v[150:153], v[34:37], v[74:77]
	ds_read_b128 v[150:153], v147 offset:8704
	ds_read_b128 v[162:165], v147 offset:8768
	s_waitcnt lgkmcnt(1)
	v_mfma_f32_16x16x32_bf16 v[70:73], v[150:153], v[34:37], v[70:73]
	ds_read_b128 v[150:153], v147 offset:13056
	ds_read_b128 v[166:169], v147 offset:13120
	s_waitcnt lgkmcnt(1)
	v_mfma_f32_16x16x32_bf16 v[66:69], v[150:153], v[34:37], v[66:69]
	ds_read_b128 v[150:153], v147 offset:17408
	ds_read_b128 v[170:173], v147 offset:17472
	s_waitcnt lgkmcnt(1)
	v_mfma_f32_16x16x32_bf16 v[62:65], v[150:153], v[34:37], v[62:65]
	ds_read_b128 v[150:153], v147 offset:21760
	ds_read_b128 v[174:177], v147 offset:21824
	s_waitcnt lgkmcnt(1)
	v_mfma_f32_16x16x32_bf16 v[58:61], v[150:153], v[34:37], v[58:61]
	ds_read_b128 v[150:153], v147 offset:26112
	ds_read_b128 v[178:181], v147 offset:26176
	s_waitcnt lgkmcnt(1)
	v_mfma_f32_16x16x32_bf16 v[54:57], v[150:153], v[34:37], v[54:57]
	ds_read_b128 v[150:153], v147 offset:30464
	ds_read_b128 v[182:185], v147 offset:30528
	s_waitcnt lgkmcnt(1)
	v_mfma_f32_16x16x32_bf16 v[50:53], v[150:153], v[34:37], v[50:53]
	v_mfma_f32_16x16x32_bf16 v[78:81], v[154:157], v[38:41], v[78:81]
	ds_read_b128 v[150:153], v147 offset:128
	ds_read_b128 v[154:157], v147 offset:192
	v_mfma_f32_16x16x32_bf16 v[74:77], v[158:161], v[38:41], v[74:77]
	s_waitcnt lgkmcnt(1)
	v_mfma_f32_16x16x32_bf16 v[78:81], v[150:153], v[42:45], v[78:81]
	ds_read_b128 v[150:153], v147 offset:4480
	ds_read_b128 v[158:161], v147 offset:4544
	v_mfma_f32_16x16x32_bf16 v[70:73], v[162:165], v[38:41], v[70:73]
	s_waitcnt lgkmcnt(1)
	v_mfma_f32_16x16x32_bf16 v[74:77], v[150:153], v[42:45], v[74:77]
	ds_read_b128 v[150:153], v147 offset:8832
	ds_read_b128 v[162:165], v147 offset:8896
	v_mfma_f32_16x16x32_bf16 v[66:69], v[166:169], v[38:41], v[66:69]
	s_waitcnt lgkmcnt(1)
	v_mfma_f32_16x16x32_bf16 v[70:73], v[150:153], v[42:45], v[70:73]
	ds_read_b128 v[150:153], v147 offset:13184
	ds_read_b128 v[166:169], v147 offset:13248
	v_mfma_f32_16x16x32_bf16 v[62:65], v[170:173], v[38:41], v[62:65]
	s_waitcnt lgkmcnt(1)
	v_mfma_f32_16x16x32_bf16 v[66:69], v[150:153], v[42:45], v[66:69]
	ds_read_b128 v[150:153], v147 offset:17536
	ds_read_b128 v[170:173], v147 offset:17600
	v_mfma_f32_16x16x32_bf16 v[58:61], v[174:177], v[38:41], v[58:61]
	s_waitcnt lgkmcnt(1)
	v_mfma_f32_16x16x32_bf16 v[62:65], v[150:153], v[42:45], v[62:65]
	ds_read_b128 v[150:153], v147 offset:21888
	ds_read_b128 v[174:177], v147 offset:21952
	v_mfma_f32_16x16x32_bf16 v[54:57], v[178:181], v[38:41], v[54:57]
	s_waitcnt lgkmcnt(1)
	v_mfma_f32_16x16x32_bf16 v[58:61], v[150:153], v[42:45], v[58:61]
	ds_read_b128 v[150:153], v147 offset:26240
	ds_read_b128 v[178:181], v147 offset:26304
	v_mfma_f32_16x16x32_bf16 v[50:53], v[182:185], v[38:41], v[50:53]
	s_waitcnt lgkmcnt(1)
	v_mfma_f32_16x16x32_bf16 v[54:57], v[150:153], v[42:45], v[54:57]
	ds_read_b128 v[150:153], v147 offset:30592
	ds_read_b128 v[182:185], v147 offset:30656
	s_waitcnt lgkmcnt(1)
	v_mfma_f32_16x16x32_bf16 v[50:53], v[150:153], v[42:45], v[50:53]
	v_mfma_f32_16x16x32_bf16 v[78:81], v[154:157], v[46:49], v[78:81]
	v_mfma_f32_16x16x32_bf16 v[74:77], v[158:161], v[46:49], v[74:77]
	v_mfma_f32_16x16x32_bf16 v[70:73], v[162:165], v[46:49], v[70:73]
	v_mfma_f32_16x16x32_bf16 v[66:69], v[166:169], v[46:49], v[66:69]
	v_mfma_f32_16x16x32_bf16 v[62:65], v[170:173], v[46:49], v[62:65]
	v_mfma_f32_16x16x32_bf16 v[58:61], v[174:177], v[46:49], v[58:61]
	v_mfma_f32_16x16x32_bf16 v[54:57], v[178:181], v[46:49], v[54:57]
	s_waitcnt lgkmcnt(0)
	v_mfma_f32_16x16x32_bf16 v[50:53], v[182:185], v[46:49], v[50:53]
	s_branch .LBB0_398
	s_nop 0
	s_nop 0
	s_nop 0
	s_nop 0
	s_nop 0
	s_nop 0
	s_nop 0
	s_nop 0
	s_nop 0
	s_nop 0
	s_nop 0
	s_nop 0
	s_nop 0
	s_nop 0
	s_nop 0
	s_nop 0
	s_nop 0
	s_nop 0
	s_nop 0
	s_nop 0
	s_nop 0
	s_nop 0
	s_nop 0
	s_nop 0
	s_nop 0
	s_nop 0
	s_nop 0
	s_nop 0
	s_nop 0
	s_nop 0
	s_nop 0
	s_nop 0
	s_nop 0
	s_nop 0
	s_nop 0
	s_nop 0
	s_nop 0
	s_nop 0
	s_nop 0
	s_nop 0
	s_nop 0
	s_nop 0
	s_nop 0
	s_nop 0

.LBB0_546:
	s_mov_b64 s[18:19], 0x80
	s_add_i32 m0, s5, 0x18000
	v_lshl_add_u64 v[134:135], v[134:135], 0, s[18:19]
	s_lshl_b32 s11, s49, 13
	s_lshl_b32 s20, s7, 7
	s_waitcnt vmcnt(2)
	s_barrier
	global_load_lds_dwordx4 v[134:135], off
	s_add_i32 m0, s5, 0x1a000
	s_add_u32 s2, s74, 0x80
	v_lshl_add_u64 v[132:133], v[132:133], 0, s[18:19]
	s_addc_u32 s3, s75, 0
	s_add_i32 s49, s5, 0x8000
	global_load_lds_dwordx4 v[132:133], off
	s_mov_b32 m0, s49
	v_lshl_add_u64 v[132:133], s[2:3], 0, v[198:199]
	s_add_i32 s50, s5, 0xa000
	global_load_lds_dwordx4 v[132:133], off
	v_lshl_add_u64 v[132:133], s[2:3], 0, v[202:203]
	s_add_u32 s2, s12, 0x80080
	s_mov_b32 m0, s50
	s_addc_u32 s3, s13, 0
	global_load_lds_dwordx4 v[132:133], off
	s_add_i32 m0, s5, 0x1c000
	v_lshl_add_u64 v[132:133], s[2:3], 0, v[208:209]
	global_load_lds_dwordx4 v[132:133], off
	v_lshl_add_u64 v[132:133], s[2:3], 0, v[206:207]
	s_add_i32 m0, s5, 0x1e000
	v_or_b32_e32 v199, s51, v137
	global_load_lds_dwordx4 v[132:133], off
	v_lshlrev_b32_e32 v132, 6, v199
	v_lshlrev_b32_e32 v133, 1, v136
	s_movk_i32 s2, 0x3c0
	v_lshlrev_b32_e32 v134, 2, v199
	v_and_or_b32 v132, v132, s2, v133
	v_and_b32_e32 v134, 32, v134
	v_bitop3_b32 v132, v132, s11, v134 bitop3:0xde
	v_lshlrev_b32_e32 v134, 6, v0
	s_waitcnt vmcnt(6)
	v_and_or_b32 v133, v134, s2, v133
	v_and_b32_e32 v134, 32, v194
	s_mov_b32 s11, 0
	s_cmpk_lt_u32 s33, 0x100
	v_bitop3_b32 v203, s20, v133, v134 bitop3:0xf6
	s_cselect_b64 s[20:21], -1, 0
	v_lshl_add_u64 v[212:213], v[130:131], 0, s[10:11]
	v_mov_b32_e32 v197, 0
	v_or_b32_e32 v214, s7, v136
	s_add_i32 s10, s5, 0xc000
	s_add_i32 s51, s5, 0xe000
	s_mov_b32 s52, 0x10000
	s_mov_b32 s53, 0xc3dc0000
	s_mov_b64 s[22:23], 0x10000
	s_mov_b64 s[24:25], 0x20000
	s_mov_b32 s54, 0x20000
	s_mov_b64 s[26:27], 0x40000
	s_mov_b32 s55, 0x40000
	v_add_u32_e32 v215, 0, v132
	v_mov_b32_e32 v223, 0x43dc0000
	v_mov_b64_e32 v[216:217], 0x1ff
	v_mov_b32_e32 v224, 1
	s_barrier
	s_branch .LBB0_548
	s_nop 0
	s_nop 0
	s_nop 0
	s_nop 0
	s_nop 0
	s_nop 0
	s_nop 0
	s_nop 0
	s_nop 0
	s_nop 0
	s_nop 0
	s_nop 0
	s_nop 0
	s_nop 0
	s_nop 0
	s_nop 0
	s_nop 0
	s_nop 0
	s_nop 0
	s_nop 0
	s_nop 0
	s_nop 0
	s_nop 0
	s_nop 0
	s_nop 0
	s_nop 0
	s_nop 0
	s_nop 0
	s_nop 0
	s_nop 0
	s_nop 0
	s_nop 0
	s_nop 0
	s_nop 0
	s_nop 0
	s_nop 0
	s_nop 0
	s_nop 0
	s_nop 0
	s_nop 0
	s_nop 0
	s_nop 0
	s_nop 0
	s_nop 0
	s_nop 0
	s_nop 0
	s_nop 0
	s_nop 0
	s_nop 0
	s_nop 0
	s_nop 0
	s_nop 0
	s_nop 0
	s_nop 0
	s_nop 0
	s_nop 0
	s_nop 0
	s_nop 0
	s_nop 0
	s_nop 0
	s_nop 0
	s_nop 0
	s_nop 0
